# ssd_out<false> epilogue: Y tile transposed through the wave's dead x LDS slice, 16 scattered 8B/lane stores -> 8 coalesced dwordx4 full-line stores
# speedup vs baseline: 1.0233x; 1.0015x over previous
.LBB0_1237:
	s_or_b64 exec, exec, s[0:1]
	v_lshl_add_u64 v[0:1], s[14:15], 2, v[170:171]
	s_waitcnt lgkmcnt(0)
	s_waitcnt lgkmcnt(0)
	s_barrier
	v_or_b32_e32 v242, s55, v167
	v_and_b32_e32 v243, 7, v219
	v_lshlrev_b32_e32 v243, 4, v243
	s_lshl_b32 s100, s14, 1
	v_lshl_add_u32 v242, v242, 13, v243
	v_add_u32_e32 v244, v209, v160
	v_add_u32_e32 v242, s100, v242
	v_add_u32_e32 v245, v211, v160
	v_add_u32_e32 v246, v212, v160
	v_add_u32_e32 v247, v210, v160
	global_load_dwordx4 v[12:15], v[0:1], off
	global_load_dwordx4 v[8:11], v[0:1], off offset:64
	global_load_dwordx4 v[4:7], v[0:1], off offset:128
	s_nop 0
	global_load_dwordx4 v[0:3], v[0:1], off offset:192
	v_lshl_add_u32 v116, v166, 2, s16
	ds_read2_b32 v[96:97], v116 offset1:16
	ds_read2_b32 v[98:99], v116 offset0:64 offset1:80
	ds_read2_b32 v[100:101], v116 offset0:128 offset1:144
	ds_read2_b32 v[102:103], v116 offset0:192 offset1:208
	v_add_u32_e32 v117, 0x400, v116
	s_waitcnt lgkmcnt(3)
	v_mov_b32_e32 v114, v97
	v_mov_b32_e32 v115, v96
	s_waitcnt lgkmcnt(2)
	v_mov_b32_e32 v96, v99
	v_mov_b32_e32 v97, v98
	s_waitcnt lgkmcnt(1)
	v_mov_b32_e32 v98, v101
	v_mov_b32_e32 v99, v100
	s_waitcnt lgkmcnt(0)
	v_mov_b32_e32 v100, v103
	v_mov_b32_e32 v101, v102
	v_pk_add_f32 v[102:103], v[114:115], 0 op_sel_hi:[1,0]
	ds_read2_b32 v[106:107], v117 offset1:16
	ds_read2_b32 v[108:109], v117 offset0:64 offset1:80
	ds_read2_b32 v[110:111], v117 offset0:128 offset1:144
	ds_read2_b32 v[112:113], v117 offset0:192 offset1:208
	v_pk_add_f32 v[96:97], v[102:103], v[96:97]
	s_waitcnt lgkmcnt(3)
	v_mov_b32_e32 v114, v107
	v_pk_add_f32 v[96:97], v[96:97], v[98:99]
	v_mov_b32_e32 v115, v106
	v_pk_add_f32 v[96:97], v[96:97], v[100:101]
	s_waitcnt lgkmcnt(2)
	v_mov_b32_e32 v106, v109
	v_mov_b32_e32 v107, v108
	v_pk_add_f32 v[96:97], v[96:97], v[114:115]
	s_waitcnt lgkmcnt(1)
	v_mov_b32_e32 v108, v111
	v_mov_b32_e32 v109, v110
	v_pk_add_f32 v[96:97], v[96:97], v[106:107]
	s_mov_b32 s0, 0x358637bd
	s_waitcnt lgkmcnt(0)
	v_mov_b32_e32 v110, v113
	v_mov_b32_e32 v111, v112
	v_pk_add_f32 v[96:97], v[96:97], v[108:109]
	v_mov_b64_e32 v[80:81], s[0:1]
	v_pk_add_f32 v[96:97], v[96:97], v[110:111]
	s_mov_b32 s16, 0x3b000000
	v_or_b32_e32 v78, s14, v162
	v_pk_fma_f32 v[96:97], v[96:97], s[16:17], v[80:81] op_sel_hi:[1,0,0]
	s_mov_b32 s14, 0x800000
	v_mul_f32_e32 v32, 0x4b800000, v97
	v_cmp_gt_f32_e64 s[0:1], s14, v97
	v_ashrrev_i32_e32 v175, 31, v174
	v_lshlrev_b64 v[104:105], 13, v[174:175]
	v_cndmask_b32_e64 v32, v97, v32, s[0:1]
	v_rsq_f32_e32 v32, v32
	v_ashrrev_i32_e32 v79, 31, v78
	v_lshl_add_u64 v[98:99], s[10:11], 0, v[104:105]
	v_lshlrev_b64 v[78:79], 1, v[78:79]
	v_mul_f32_e32 v97, 0x45800000, v32
	v_cndmask_b32_e64 v32, v32, v97, s[0:1]
	v_pk_mul_f32 v[66:67], v[66:67], v[32:33] op_sel_hi:[1,0]
	v_pk_mul_f32 v[68:69], v[68:69], v[32:33] op_sel_hi:[1,0]
	v_pk_mul_f32 v[62:63], v[62:63], v[32:33] op_sel_hi:[1,0]
	v_pk_mul_f32 v[64:65], v[64:65], v[32:33] op_sel_hi:[1,0]
	v_pk_mul_f32 v[58:59], v[58:59], v[32:33] op_sel_hi:[1,0]
	v_pk_mul_f32 v[60:61], v[60:61], v[32:33] op_sel_hi:[1,0]
	v_pk_mul_f32 v[72:73], v[72:73], v[32:33] op_sel_hi:[1,0]
	v_pk_mul_f32 v[56:57], v[56:57], v[32:33] op_sel_hi:[1,0]
	v_mul_f32_e32 v32, 0x4b800000, v96
	v_cmp_gt_f32_e64 s[0:1], s14, v96
	v_lshl_add_u64 v[98:99], v[98:99], 0, v[78:79]
	v_ashrrev_i32_e32 v55, 31, v54
	v_cndmask_b32_e64 v32, v96, v32, s[0:1]
	v_rsq_f32_e32 v32, v32
	v_lshlrev_b64 v[54:55], 13, v[54:55]
	v_lshl_add_u64 v[54:55], s[10:11], 0, v[54:55]
	v_ashrrev_i32_e32 v77, 31, v76
	v_ashrrev_i32_e32 v75, 31, v74
	s_add_i32 s54, s54, s94
	s_xor_b32 s33, s33, 1
	s_cmpk_lt_i32 s54, 0x400
	s_waitcnt vmcnt(3)
	v_pk_mul_f32 v[68:69], v[14:15], v[68:69]
	v_pk_mul_f32 v[66:67], v[12:13], v[66:67]
	s_waitcnt vmcnt(1)
	v_pk_mul_f32 v[60:61], v[6:7], v[60:61]
	v_pk_mul_f32 v[58:59], v[4:5], v[58:59]
	v_pk_mul_f32 v[64:65], v[10:11], v[64:65]
	v_pk_mul_f32 v[62:63], v[8:9], v[62:63]
	v_cvt_pk_bf16_f32 v66, v66, v67
	v_cvt_pk_bf16_f32 v67, v68, v69
	v_cvt_pk_bf16_f32 v58, v58, v59
	v_cvt_pk_bf16_f32 v59, v60, v61
	v_cvt_pk_bf16_f32 v62, v62, v63
	v_cvt_pk_bf16_f32 v63, v64, v65
	ds_write_b64 v244, v[66:67]
	ds_write_b64 v244, v[62:63] offset:32
	ds_write_b64 v244, v[58:59] offset:64
	s_waitcnt vmcnt(0)
	v_pk_mul_f32 v[56:57], v[2:3], v[56:57]
	v_pk_mul_f32 v[58:59], v[0:1], v[72:73]
	s_nop 0
	v_cvt_pk_bf16_f32 v58, v58, v59
	v_cvt_pk_bf16_f32 v59, v56, v57
	v_mul_f32_e32 v56, 0x45800000, v32
	v_cndmask_b32_e64 v32, v32, v56, s[0:1]
	v_pk_mul_f32 v[50:51], v[50:51], v[32:33] op_sel_hi:[1,0]
	v_pk_mul_f32 v[52:53], v[52:53], v[32:33] op_sel_hi:[1,0]
	v_pk_mul_f32 v[46:47], v[46:47], v[32:33] op_sel_hi:[1,0]
	v_pk_mul_f32 v[48:49], v[48:49], v[32:33] op_sel_hi:[1,0]
	v_pk_mul_f32 v[42:43], v[42:43], v[32:33] op_sel_hi:[1,0]
	v_pk_mul_f32 v[44:45], v[44:45], v[32:33] op_sel_hi:[1,0]
	v_pk_mul_f32 v[28:29], v[28:29], v[32:33] op_sel_hi:[1,0]
	v_pk_mul_f32 v[30:31], v[30:31], v[32:33] op_sel_hi:[1,0]
	v_pk_mul_f32 v[52:53], v[14:15], v[52:53]
	v_pk_mul_f32 v[50:51], v[12:13], v[50:51]
	v_pk_mul_f32 v[48:49], v[10:11], v[48:49]
	v_pk_mul_f32 v[46:47], v[8:9], v[46:47]
	v_pk_mul_f32 v[44:45], v[6:7], v[44:45]
	v_pk_mul_f32 v[42:43], v[4:5], v[42:43]
	v_pk_mul_f32 v[30:31], v[2:3], v[30:31]
	v_pk_mul_f32 v[28:29], v[0:1], v[28:29]
	v_cvt_pk_bf16_f32 v50, v50, v51
	v_cvt_pk_bf16_f32 v51, v52, v53
	v_lshl_add_u64 v[52:53], v[54:55], 0, v[78:79]
	v_cvt_pk_bf16_f32 v46, v46, v47
	v_cvt_pk_bf16_f32 v47, v48, v49
	v_cvt_pk_bf16_f32 v42, v42, v43
	v_cvt_pk_bf16_f32 v43, v44, v45
	v_cvt_pk_bf16_f32 v28, v28, v29
	v_cvt_pk_bf16_f32 v29, v30, v31
	ds_write_b64 v244, v[58:59] offset:96
	ds_write_b64 v245, v[50:51]
	ds_write_b64 v245, v[46:47] offset:32
	ds_write_b64 v245, v[42:43] offset:64
	ds_write_b64 v245, v[28:29] offset:96
	ds_read2_b32 v[28:29], v116 offset0:32 offset1:48
	ds_read2_b32 v[30:31], v116 offset0:96 offset1:112
	ds_read2_b32 v[42:43], v116 offset0:160 offset1:176
	ds_read2_b32 v[44:45], v116 offset0:224 offset1:240
	ds_read2_b32 v[46:47], v117 offset0:32 offset1:48
	ds_read2_b32 v[48:49], v117 offset0:96 offset1:112
	ds_read2_b32 v[50:51], v117 offset0:160 offset1:176
	ds_read2_b32 v[52:53], v117 offset0:224 offset1:240
	s_waitcnt lgkmcnt(7)
	v_mov_b32_e32 v54, v29
	v_mov_b32_e32 v55, v28
	v_pk_add_f32 v[28:29], v[54:55], 0 op_sel_hi:[1,0]
	s_waitcnt lgkmcnt(6)
	v_mov_b32_e32 v54, v31
	v_mov_b32_e32 v55, v30
	v_pk_add_f32 v[28:29], v[28:29], v[54:55]
	s_waitcnt lgkmcnt(5)
	v_mov_b32_e32 v30, v43
	v_mov_b32_e32 v31, v42
	v_pk_add_f32 v[28:29], v[28:29], v[30:31]
	s_waitcnt lgkmcnt(4)
	v_mov_b32_e32 v30, v45
	v_mov_b32_e32 v31, v44
	v_pk_add_f32 v[28:29], v[28:29], v[30:31]
	s_waitcnt lgkmcnt(3)
	v_mov_b32_e32 v30, v47
	v_mov_b32_e32 v31, v46
	v_pk_add_f32 v[28:29], v[28:29], v[30:31]
	s_waitcnt lgkmcnt(2)
	v_mov_b32_e32 v30, v49
	v_mov_b32_e32 v31, v48
	v_pk_add_f32 v[28:29], v[28:29], v[30:31]
	s_waitcnt lgkmcnt(1)
	v_mov_b32_e32 v30, v51
	v_mov_b32_e32 v31, v50
	v_pk_add_f32 v[28:29], v[28:29], v[30:31]
	s_waitcnt lgkmcnt(0)
	v_mov_b32_e32 v30, v53
	v_mov_b32_e32 v31, v52
	v_pk_add_f32 v[28:29], v[28:29], v[30:31]
	s_nop 0
	v_pk_fma_f32 v[28:29], v[28:29], s[16:17], v[80:81] op_sel_hi:[1,0,0]
	s_nop 0
	v_mul_f32_e32 v30, 0x4b800000, v29
	v_cmp_gt_f32_e64 s[0:1], s14, v29
	s_nop 1
	v_cndmask_b32_e64 v29, v29, v30, s[0:1]
	v_rsq_f32_e32 v29, v29
	v_lshlrev_b64 v[30:31], 13, v[76:77]
	v_lshl_add_u64 v[30:31], s[10:11], 0, v[30:31]
	v_lshl_add_u64 v[30:31], v[30:31], 0, v[78:79]
	v_mul_f32_e32 v32, 0x45800000, v29
	v_cndmask_b32_e64 v32, v29, v32, s[0:1]
	v_pk_mul_f32 v[20:21], v[20:21], v[32:33] op_sel_hi:[1,0]
	v_pk_mul_f32 v[22:23], v[22:23], v[32:33] op_sel_hi:[1,0]
	v_pk_mul_f32 v[20:21], v[8:9], v[20:21]
	v_pk_mul_f32 v[22:23], v[10:11], v[22:23]
	v_cvt_pk_bf16_f32 v20, v20, v21
	v_cvt_pk_bf16_f32 v21, v22, v23
	ds_write_b64 v246, v[20:21] offset:32
	v_pk_mul_f32 v[16:17], v[16:17], v[32:33] op_sel_hi:[1,0]
	v_pk_mul_f32 v[18:19], v[18:19], v[32:33] op_sel_hi:[1,0]
	v_mul_f32_e32 v20, 0x4b800000, v28
	v_cmp_gt_f32_e64 s[0:1], s14, v28
	v_pk_mul_f32 v[18:19], v[6:7], v[18:19]
	v_pk_mul_f32 v[16:17], v[4:5], v[16:17]
	v_cndmask_b32_e64 v20, v28, v20, s[0:1]
	v_cvt_pk_bf16_f32 v16, v16, v17
	v_cvt_pk_bf16_f32 v17, v18, v19
	v_rsq_f32_e32 v20, v20
	ds_write_b64 v246, v[16:17] offset:64
	v_pk_mul_f32 v[16:17], v[24:25], v[32:33] op_sel_hi:[1,0]
	v_pk_mul_f32 v[18:19], v[26:27], v[32:33] op_sel_hi:[1,0]
	v_pk_mul_f32 v[16:17], v[0:1], v[16:17]
	v_pk_mul_f32 v[18:19], v[2:3], v[18:19]
	v_cvt_pk_bf16_f32 v16, v16, v17
	v_cvt_pk_bf16_f32 v17, v18, v19
	ds_write_b64 v246, v[16:17] offset:96
	v_mul_f32_e32 v16, 0x45800000, v20
	v_cndmask_b32_e64 v16, v20, v16, s[0:1]
	v_pk_mul_f32 v[38:39], v[38:39], v[32:33] op_sel_hi:[1,0]
	v_pk_mul_f32 v[40:41], v[40:41], v[32:33] op_sel_hi:[1,0]
	v_lshlrev_b64 v[18:19], 13, v[74:75]
	v_pk_mul_f32 v[20:21], v[94:95], v[16:17] op_sel_hi:[1,0]
	v_pk_mul_f32 v[22:23], v[90:91], v[16:17] op_sel_hi:[1,0]
	v_pk_mul_f32 v[40:41], v[14:15], v[40:41]
	v_pk_mul_f32 v[38:39], v[12:13], v[38:39]
	v_lshl_add_u64 v[18:19], s[10:11], 0, v[18:19]
	v_pk_mul_f32 v[14:15], v[14:15], v[22:23]
	v_pk_mul_f32 v[12:13], v[12:13], v[20:21]
	v_cvt_pk_bf16_f32 v38, v38, v39
	v_cvt_pk_bf16_f32 v12, v12, v13
	v_cvt_pk_bf16_f32 v13, v14, v15
	v_lshl_add_u64 v[14:15], v[18:19], 0, v[78:79]
	ds_write_b64 v247, v[12:13]
	v_pk_mul_f32 v[12:13], v[92:93], v[16:17] op_sel_hi:[1,0]
	v_pk_mul_f32 v[18:19], v[86:87], v[16:17] op_sel_hi:[1,0]
	v_pk_mul_f32 v[8:9], v[8:9], v[12:13]
	v_pk_mul_f32 v[10:11], v[10:11], v[18:19]
	v_cvt_pk_bf16_f32 v8, v8, v9
	v_cvt_pk_bf16_f32 v9, v10, v11
	ds_write_b64 v247, v[8:9] offset:32
	v_pk_mul_f32 v[8:9], v[88:89], v[16:17] op_sel_hi:[1,0]
	v_pk_mul_f32 v[10:11], v[82:83], v[16:17] op_sel_hi:[1,0]
	v_pk_mul_f32 v[4:5], v[4:5], v[8:9]
	v_pk_mul_f32 v[6:7], v[6:7], v[10:11]
	v_cvt_pk_bf16_f32 v4, v4, v5
	v_cvt_pk_bf16_f32 v5, v6, v7
	ds_write_b64 v247, v[4:5] offset:64
	v_pk_mul_f32 v[4:5], v[84:85], v[16:17] op_sel_hi:[1,0]
	v_pk_mul_f32 v[6:7], v[70:71], v[16:17] op_sel_hi:[1,0]
	v_pk_mul_f32 v[0:1], v[0:1], v[4:5]
	v_pk_mul_f32 v[2:3], v[2:3], v[6:7]
	v_cvt_pk_bf16_f32 v39, v40, v41
	v_cvt_pk_bf16_f32 v0, v0, v1
	v_cvt_pk_bf16_f32 v1, v2, v3
	ds_write_b64 v246, v[38:39]
	ds_write_b64 v247, v[0:1] offset:96
	s_waitcnt lgkmcnt(0)
	ds_read_b128 v[0:3], v213
	ds_read_b128 v[4:7], v213 offset:1280
	ds_read_b128 v[8:11], v213 offset:2560
	ds_read_b128 v[12:15], v213 offset:3840
	ds_read_b128 v[16:19], v213 offset:5120
	ds_read_b128 v[20:23], v213 offset:6400
	ds_read_b128 v[24:27], v213 offset:7680
	ds_read_b128 v[28:31], v213 offset:8960
	s_waitcnt lgkmcnt(7)
	global_store_dwordx4 v242, v[0:3], s[10:11]
	v_add_u32_e32 v242, 0x10000, v242
	s_waitcnt lgkmcnt(6)
	global_store_dwordx4 v242, v[4:7], s[10:11]
	v_add_u32_e32 v242, 0x10000, v242
	s_waitcnt lgkmcnt(5)
	global_store_dwordx4 v242, v[8:11], s[10:11]
	v_add_u32_e32 v242, 0x10000, v242
	s_waitcnt lgkmcnt(4)
	global_store_dwordx4 v242, v[12:15], s[10:11]
	v_add_u32_e32 v242, 0x10000, v242
	s_waitcnt lgkmcnt(3)
	global_store_dwordx4 v242, v[16:19], s[10:11]
	v_add_u32_e32 v242, 0x10000, v242
	s_waitcnt lgkmcnt(2)
	global_store_dwordx4 v242, v[20:23], s[10:11]
	v_add_u32_e32 v242, 0x10000, v242
	s_waitcnt lgkmcnt(1)
	global_store_dwordx4 v242, v[24:27], s[10:11]
	v_add_u32_e32 v242, 0x10000, v242
	s_waitcnt lgkmcnt(0)
	global_store_dwordx4 v242, v[28:31], s[10:11]
	s_nop 1
	s_cbranch_scc0 .LBB0_1246
